# speedup vs baseline: 1.0204x; 1.0053x over previous
.LBB2_356:
	ds_read_b128 v[140:143], v138
	ds_read_b128 v[154:157], v138 offset:1024
	ds_read_b128 v[158:161], v138 offset:2048
	ds_read_b128 v[164:167], v138 offset:3072
	s_lshl_b32 vcc_hi, s57, 7
	s_add_u32 s58, s88, vcc_hi
	s_addc_u32 s59, s89, 0
	s_add_u32 s82, s58, 0x80
	s_addc_u32 s83, s59, 0
	s_add_i32 s59, s97, 0xc000
	s_mov_b32 m0, s59
	s_add_i32 s58, s97, 0xe000
	ds_read_b128 v[168:171], v134
	ds_read_b128 v[172:175], v134 offset:1024
	ds_read_b128 v[176:179], v133
	ds_read_b128 v[184:187], v133 offset:1024
	ds_read_b128 v[188:191], v131
	ds_read_b128 v[192:195], v131 offset:1024
	ds_read_b128 v[196:199], v130
	ds_read_b128 v[200:203], v130 offset:1024
	global_load_lds_dwordx4 v162, s[82:83]
	s_mov_b32 m0, s58
	s_add_u32 s82, s82, 0x20000
	s_addc_u32 s83, s83, 0
	global_load_lds_dwordx4 v162, s[82:83]
	s_waitcnt lgkmcnt(8)
	s_barrier
	s_waitcnt lgkmcnt(0)
	v_mfma_f32_16x16x32_f16 v[102:105], v[140:143], v[168:171], v[102:105]
	v_mfma_f32_16x16x32_f16 v[98:101], v[158:161], v[168:171], v[98:101]
	v_mfma_f32_16x16x32_f16 v[126:129], v[140:143], v[176:179], v[126:129]
	v_mfma_f32_16x16x32_f16 v[122:125], v[158:161], v[176:179], v[122:125]
	v_mfma_f32_16x16x32_f16 v[118:121], v[140:143], v[188:191], v[118:121]
	v_mfma_f32_16x16x32_f16 v[114:117], v[158:161], v[188:191], v[114:117]
	v_mfma_f32_16x16x32_f16 v[110:113], v[140:143], v[196:199], v[110:113]
	v_mfma_f32_16x16x32_f16 v[106:109], v[158:161], v[196:199], v[106:109]
	v_mfma_f32_16x16x32_f16 v[102:105], v[154:157], v[172:175], v[102:105]
	v_mfma_f32_16x16x32_f16 v[98:101], v[164:167], v[172:175], v[98:101]
	v_mfma_f32_16x16x32_f16 v[126:129], v[154:157], v[184:187], v[126:129]
	v_mfma_f32_16x16x32_f16 v[122:125], v[164:167], v[184:187], v[122:125]
	v_mfma_f32_16x16x32_f16 v[118:121], v[154:157], v[192:195], v[118:121]
	v_mfma_f32_16x16x32_f16 v[114:117], v[164:167], v[192:195], v[114:117]
	v_mfma_f32_16x16x32_f16 v[110:113], v[154:157], v[200:203], v[110:113]
	v_mfma_f32_16x16x32_f16 v[106:109], v[164:167], v[200:203], v[106:109]
	s_barrier
	s_add_i32 vcc_lo, s57, 2
	s_lshl_b32 s78, vcc_lo, 7
	s_add_u32 s82, s92, s78
	s_addc_u32 s83, s93, 0
	s_mov_b32 m0, s84
	ds_read_b128 v[204:207], v137
	ds_read_b128 v[208:211], v137 offset:1024
	ds_read_b128 v[212:215], v137 offset:2048
	ds_read_b128 v[216:219], v137 offset:3072
	global_load_lds_dwordx4 v162, s[82:83]
	s_mov_b32 m0, s94
	s_add_u32 s82, s82, 0x20000
	s_addc_u32 s83, s83, 0
	global_load_lds_dwordx4 v162, s[82:83]
	s_barrier
	s_waitcnt lgkmcnt(0)
	v_mfma_f32_16x16x32_f16 v[94:97], v[204:207], v[168:171], v[94:97]
	v_mfma_f32_16x16x32_f16 v[90:93], v[212:215], v[168:171], v[90:93]
	v_mfma_f32_16x16x32_f16 v[86:89], v[204:207], v[176:179], v[86:89]
	v_mfma_f32_16x16x32_f16 v[82:85], v[212:215], v[176:179], v[82:85]
	v_mfma_f32_16x16x32_f16 v[78:81], v[204:207], v[188:191], v[78:81]
	v_mfma_f32_16x16x32_f16 v[74:77], v[212:215], v[188:191], v[74:77]
	v_mfma_f32_16x16x32_f16 v[70:73], v[204:207], v[196:199], v[70:73]
	v_mfma_f32_16x16x32_f16 v[66:69], v[212:215], v[196:199], v[66:69]
	v_mfma_f32_16x16x32_f16 v[94:97], v[208:211], v[172:175], v[94:97]
	v_mfma_f32_16x16x32_f16 v[90:93], v[216:219], v[172:175], v[90:93]
	v_mfma_f32_16x16x32_f16 v[86:89], v[208:211], v[184:187], v[86:89]
	v_mfma_f32_16x16x32_f16 v[82:85], v[216:219], v[184:187], v[82:85]
	v_mfma_f32_16x16x32_f16 v[78:81], v[208:211], v[192:195], v[78:81]
	v_mfma_f32_16x16x32_f16 v[74:77], v[216:219], v[192:195], v[74:77]
	v_mfma_f32_16x16x32_f16 v[70:73], v[208:211], v[200:203], v[70:73]
	v_mfma_f32_16x16x32_f16 v[66:69], v[216:219], v[200:203], v[66:69]
	s_add_u32 s82, s90, s78
	s_addc_u32 s83, s91, 0
	s_mov_b32 m0, s97
	s_barrier
	ds_read_b128 v[168:171], v134 offset:16384
	ds_read_b128 v[172:175], v134 offset:17408
	ds_read_b128 v[176:179], v133 offset:16384
	ds_read_b128 v[184:187], v133 offset:17408
	ds_read_b128 v[188:191], v131 offset:16384
	ds_read_b128 v[192:195], v131 offset:17408
	ds_read_b128 v[196:199], v130 offset:16384
	ds_read_b128 v[200:203], v130 offset:17408
	global_load_lds_dwordx4 v162, s[82:83]
	s_mov_b32 m0, s99
	s_add_u32 s82, s82, 0x20000
	s_addc_u32 s83, s83, 0
	global_load_lds_dwordx4 v162, s[82:83]
	s_barrier
	s_waitcnt lgkmcnt(0)
	v_mfma_f32_16x16x32_f16 v[62:65], v[140:143], v[168:171], v[62:65]
	v_mfma_f32_16x16x32_f16 v[58:61], v[158:161], v[168:171], v[58:61]
	v_mfma_f32_16x16x32_f16 v[54:57], v[140:143], v[176:179], v[54:57]
	v_mfma_f32_16x16x32_f16 v[50:53], v[158:161], v[176:179], v[50:53]
	v_mfma_f32_16x16x32_f16 v[46:49], v[140:143], v[188:191], v[46:49]
	v_mfma_f32_16x16x32_f16 v[42:45], v[158:161], v[188:191], v[42:45]
	v_mfma_f32_16x16x32_f16 v[38:41], v[140:143], v[196:199], v[38:41]
	v_mfma_f32_16x16x32_f16 v[30:33], v[158:161], v[196:199], v[30:33]
	v_mfma_f32_16x16x32_f16 v[62:65], v[154:157], v[172:175], v[62:65]
	v_mfma_f32_16x16x32_f16 v[58:61], v[164:167], v[172:175], v[58:61]
	v_mfma_f32_16x16x32_f16 v[54:57], v[154:157], v[184:187], v[54:57]
	v_mfma_f32_16x16x32_f16 v[50:53], v[164:167], v[184:187], v[50:53]
	v_mfma_f32_16x16x32_f16 v[46:49], v[154:157], v[192:195], v[46:49]
	v_mfma_f32_16x16x32_f16 v[42:45], v[164:167], v[192:195], v[42:45]
	v_mfma_f32_16x16x32_f16 v[38:41], v[154:157], v[200:203], v[38:41]
	v_mfma_f32_16x16x32_f16 v[30:33], v[164:167], v[200:203], v[30:33]
	s_barrier
	s_add_u32 s82, s34, s78
	s_addc_u32 s83, s35, 0
	s_mov_b32 m0, s95
	s_nop 0
	global_load_lds_dwordx4 v162, s[82:83]
	s_mov_b32 m0, s33
	s_add_u32 s82, s82, 0x20000
	s_addc_u32 s83, s83, 0
	global_load_lds_dwordx4 v162, s[82:83]
	s_waitcnt vmcnt(6)
	s_barrier
	v_mfma_f32_16x16x32_f16 v[34:37], v[204:207], v[168:171], v[34:37]
	v_mfma_f32_16x16x32_f16 v[26:29], v[212:215], v[168:171], v[26:29]
	v_mfma_f32_16x16x32_f16 v[22:25], v[204:207], v[176:179], v[22:25]
	v_mfma_f32_16x16x32_f16 v[18:21], v[212:215], v[176:179], v[18:21]
	v_mfma_f32_16x16x32_f16 v[14:17], v[204:207], v[188:191], v[14:17]
	v_mfma_f32_16x16x32_f16 v[10:13], v[212:215], v[188:191], v[10:13]
	v_mfma_f32_16x16x32_f16 v[6:9], v[204:207], v[196:199], v[6:9]
	v_mfma_f32_16x16x32_f16 v[2:5], v[212:215], v[196:199], v[2:5]
	v_mfma_f32_16x16x32_f16 v[34:37], v[208:211], v[172:175], v[34:37]
	v_mfma_f32_16x16x32_f16 v[26:29], v[216:219], v[172:175], v[26:29]
	v_mfma_f32_16x16x32_f16 v[22:25], v[208:211], v[184:187], v[22:25]
	v_mfma_f32_16x16x32_f16 v[18:21], v[216:219], v[184:187], v[18:21]
	v_mfma_f32_16x16x32_f16 v[14:17], v[208:211], v[192:195], v[14:17]
	v_mfma_f32_16x16x32_f16 v[10:13], v[216:219], v[192:195], v[10:13]
	v_mfma_f32_16x16x32_f16 v[6:9], v[208:211], v[200:203], v[6:9]
	v_mfma_f32_16x16x32_f16 v[2:5], v[216:219], v[200:203], v[2:5]
	s_barrier
	ds_read_b128 v[140:143], v136
	ds_read_b128 v[154:157], v136 offset:1024
	ds_read_b128 v[158:161], v136 offset:2048
	ds_read_b128 v[164:167], v136 offset:3072
	s_add_u32 s82, s88, s78
	s_addc_u32 s83, s89, 0
	s_mov_b32 m0, s11
	ds_read_b128 v[168:171], v134 offset:32768
	ds_read_b128 v[172:175], v134 offset:33792
	ds_read_b128 v[176:179], v133 offset:32768
	ds_read_b128 v[184:187], v133 offset:33792
	ds_read_b128 v[188:191], v131 offset:32768
	ds_read_b128 v[192:195], v131 offset:33792
	ds_read_b128 v[196:199], v130 offset:32768
	ds_read_b128 v[200:203], v130 offset:33792
	global_load_lds_dwordx4 v162, s[82:83]
	s_mov_b32 m0, s56
	s_add_u32 s82, s82, 0x20000
	s_addc_u32 s83, s83, 0
	global_load_lds_dwordx4 v162, s[82:83]
	s_waitcnt lgkmcnt(8)
	s_barrier
	s_waitcnt lgkmcnt(0)
	v_mfma_f32_16x16x32_f16 v[102:105], v[140:143], v[168:171], v[102:105]
	v_mfma_f32_16x16x32_f16 v[98:101], v[158:161], v[168:171], v[98:101]
	v_mfma_f32_16x16x32_f16 v[126:129], v[140:143], v[176:179], v[126:129]
	v_mfma_f32_16x16x32_f16 v[122:125], v[158:161], v[176:179], v[122:125]
	v_mfma_f32_16x16x32_f16 v[118:121], v[140:143], v[188:191], v[118:121]
	v_mfma_f32_16x16x32_f16 v[114:117], v[158:161], v[188:191], v[114:117]
	v_mfma_f32_16x16x32_f16 v[110:113], v[140:143], v[196:199], v[110:113]
	v_mfma_f32_16x16x32_f16 v[106:109], v[158:161], v[196:199], v[106:109]
	v_mfma_f32_16x16x32_f16 v[102:105], v[154:157], v[172:175], v[102:105]
	v_mfma_f32_16x16x32_f16 v[98:101], v[164:167], v[172:175], v[98:101]
	v_mfma_f32_16x16x32_f16 v[126:129], v[154:157], v[184:187], v[126:129]
	v_mfma_f32_16x16x32_f16 v[122:125], v[164:167], v[184:187], v[122:125]
	v_mfma_f32_16x16x32_f16 v[118:121], v[154:157], v[192:195], v[118:121]
	v_mfma_f32_16x16x32_f16 v[114:117], v[164:167], v[192:195], v[114:117]
	v_mfma_f32_16x16x32_f16 v[110:113], v[154:157], v[200:203], v[110:113]
	v_mfma_f32_16x16x32_f16 v[106:109], v[164:167], v[200:203], v[106:109]
	s_barrier
	s_add_u32 s78, s92, vcc_hi
	s_addc_u32 s79, s93, 0
	s_add_u32 s82, s78, 0x180
	s_addc_u32 s83, s79, 0
	s_add_i32 m0, s97, 0x18000
	ds_read_b128 v[204:207], v135
	ds_read_b128 v[208:211], v135 offset:1024
	ds_read_b128 v[212:215], v135 offset:2048
	ds_read_b128 v[216:219], v135 offset:3072
	global_load_lds_dwordx4 v162, s[82:83]
	s_add_i32 m0, s97, 0x1a000
	s_add_u32 s82, s82, 0x20000
	s_addc_u32 s83, s83, 0
	global_load_lds_dwordx4 v162, s[82:83]
	s_barrier
	s_waitcnt lgkmcnt(0)
	v_mfma_f32_16x16x32_f16 v[94:97], v[204:207], v[168:171], v[94:97]
	v_mfma_f32_16x16x32_f16 v[90:93], v[212:215], v[168:171], v[90:93]
	v_mfma_f32_16x16x32_f16 v[86:89], v[204:207], v[176:179], v[86:89]
	v_mfma_f32_16x16x32_f16 v[82:85], v[212:215], v[176:179], v[82:85]
	v_mfma_f32_16x16x32_f16 v[78:81], v[204:207], v[188:191], v[78:81]
	v_mfma_f32_16x16x32_f16 v[74:77], v[212:215], v[188:191], v[74:77]
	v_mfma_f32_16x16x32_f16 v[70:73], v[204:207], v[196:199], v[70:73]
	v_mfma_f32_16x16x32_f16 v[66:69], v[212:215], v[196:199], v[66:69]
	v_mfma_f32_16x16x32_f16 v[94:97], v[208:211], v[172:175], v[94:97]
	v_mfma_f32_16x16x32_f16 v[90:93], v[216:219], v[172:175], v[90:93]
	v_mfma_f32_16x16x32_f16 v[86:89], v[208:211], v[184:187], v[86:89]
	v_mfma_f32_16x16x32_f16 v[82:85], v[216:219], v[184:187], v[82:85]
	v_mfma_f32_16x16x32_f16 v[78:81], v[208:211], v[192:195], v[78:81]
	v_mfma_f32_16x16x32_f16 v[74:77], v[216:219], v[192:195], v[74:77]
	v_mfma_f32_16x16x32_f16 v[70:73], v[208:211], v[200:203], v[70:73]
	v_mfma_f32_16x16x32_f16 v[66:69], v[216:219], v[200:203], v[66:69]
	s_add_u32 s78, s90, vcc_hi
	s_addc_u32 s79, s91, 0
	s_add_u32 s82, s78, 0x180
	s_addc_u32 s83, s79, 0
	s_mov_b32 m0, s52
	s_barrier
	ds_read_b128 v[168:171], v134 offset:49152
	ds_read_b128 v[172:175], v134 offset:50176
	ds_read_b128 v[176:179], v133 offset:49152
	ds_read_b128 v[184:187], v133 offset:50176
	ds_read_b128 v[188:191], v131 offset:49152
	ds_read_b128 v[192:195], v131 offset:50176
	ds_read_b128 v[196:199], v130 offset:49152
	ds_read_b128 v[200:203], v130 offset:50176
	global_load_lds_dwordx4 v162, s[82:83]
	s_mov_b32 m0, s53
	s_add_u32 s82, s82, 0x20000
	s_addc_u32 s83, s83, 0
	global_load_lds_dwordx4 v162, s[82:83]
	s_barrier
	s_waitcnt lgkmcnt(0)
	v_mfma_f32_16x16x32_f16 v[62:65], v[140:143], v[168:171], v[62:65]
	v_mfma_f32_16x16x32_f16 v[58:61], v[158:161], v[168:171], v[58:61]
	v_mfma_f32_16x16x32_f16 v[54:57], v[140:143], v[176:179], v[54:57]
	v_mfma_f32_16x16x32_f16 v[50:53], v[158:161], v[176:179], v[50:53]
	v_mfma_f32_16x16x32_f16 v[46:49], v[140:143], v[188:191], v[46:49]
	v_mfma_f32_16x16x32_f16 v[42:45], v[158:161], v[188:191], v[42:45]
	v_mfma_f32_16x16x32_f16 v[38:41], v[140:143], v[196:199], v[38:41]
	v_mfma_f32_16x16x32_f16 v[30:33], v[158:161], v[196:199], v[30:33]
	v_mfma_f32_16x16x32_f16 v[62:65], v[154:157], v[172:175], v[62:65]
	v_mfma_f32_16x16x32_f16 v[58:61], v[164:167], v[172:175], v[58:61]
	v_mfma_f32_16x16x32_f16 v[54:57], v[154:157], v[184:187], v[54:57]
	v_mfma_f32_16x16x32_f16 v[50:53], v[164:167], v[184:187], v[50:53]
	v_mfma_f32_16x16x32_f16 v[46:49], v[154:157], v[192:195], v[46:49]
	v_mfma_f32_16x16x32_f16 v[42:45], v[164:167], v[192:195], v[42:45]
	v_mfma_f32_16x16x32_f16 v[38:41], v[154:157], v[200:203], v[38:41]
	v_mfma_f32_16x16x32_f16 v[30:33], v[164:167], v[200:203], v[30:33]
	s_barrier
	s_add_u32 s78, s34, vcc_hi
	s_addc_u32 s79, s35, 0
	s_add_u32 s82, s78, 0x180
	s_addc_u32 s83, s79, 0
	s_add_i32 m0, s97, 0x1c000
	s_nop 0
	global_load_lds_dwordx4 v162, s[82:83]
	s_add_i32 m0, s97, 0x1e000
	s_add_u32 s82, s82, 0x20000
	s_addc_u32 s83, s83, 0
	global_load_lds_dwordx4 v162, s[82:83]
	s_waitcnt vmcnt(6)
	s_barrier
	v_mfma_f32_16x16x32_f16 v[34:37], v[204:207], v[168:171], v[34:37]
	v_mfma_f32_16x16x32_f16 v[26:29], v[212:215], v[168:171], v[26:29]
	v_mfma_f32_16x16x32_f16 v[22:25], v[204:207], v[176:179], v[22:25]
	v_mfma_f32_16x16x32_f16 v[18:21], v[212:215], v[176:179], v[18:21]
	v_mfma_f32_16x16x32_f16 v[14:17], v[204:207], v[188:191], v[14:17]
	v_mfma_f32_16x16x32_f16 v[10:13], v[212:215], v[188:191], v[10:13]
	v_mfma_f32_16x16x32_f16 v[6:9], v[204:207], v[196:199], v[6:9]
	v_mfma_f32_16x16x32_f16 v[2:5], v[212:215], v[196:199], v[2:5]
	v_mfma_f32_16x16x32_f16 v[34:37], v[208:211], v[172:175], v[34:37]
	v_mfma_f32_16x16x32_f16 v[26:29], v[216:219], v[172:175], v[26:29]
	v_mfma_f32_16x16x32_f16 v[22:25], v[208:211], v[184:187], v[22:25]
	v_mfma_f32_16x16x32_f16 v[18:21], v[216:219], v[184:187], v[18:21]
	v_mfma_f32_16x16x32_f16 v[14:17], v[208:211], v[192:195], v[14:17]
	v_mfma_f32_16x16x32_f16 v[10:13], v[216:219], v[192:195], v[10:13]
	v_mfma_f32_16x16x32_f16 v[6:9], v[208:211], v[200:203], v[6:9]
	v_mfma_f32_16x16x32_f16 v[2:5], v[216:219], v[200:203], v[2:5]
	s_cmp_lt_u32 s57, 12
	s_mov_b32 s57, vcc_lo
	s_barrier
	s_cbranch_scc1 .LBB2_356
	s_add_u32 s34, s88, 0x780
	s_addc_u32 s35, s89, 0
	ds_read_b128 v[140:143], v138
	ds_read_b128 v[154:157], v138 offset:1024
	ds_read_b128 v[158:161], v138 offset:2048
	ds_read_b128 v[164:167], v138 offset:3072
	ds_read_b128 v[168:171], v134
	ds_read_b128 v[172:175], v134 offset:1024
	ds_read_b128 v[176:179], v133
	ds_read_b128 v[184:187], v133 offset:1024
	ds_read_b128 v[188:191], v131
	ds_read_b128 v[192:195], v131 offset:1024
	ds_read_b128 v[196:199], v130
	ds_read_b128 v[200:203], v130 offset:1024
	v_lshl_add_u64 v[138:139], s[34:35], 0, v[162:163]
	s_add_u32 s34, s34, 0x20000
	s_mov_b32 m0, s59
	s_addc_u32 s35, s35, 0
	global_load_lds_dwordx4 v[138:139], off
	s_mov_b32 m0, s58
	v_lshl_add_u64 v[138:139], s[34:35], 0, v[162:163]
	global_load_lds_dwordx4 v[138:139], off
	s_barrier
	s_waitcnt lgkmcnt(0)
	v_mfma_f32_16x16x32_f16 v[102:105], v[140:143], v[168:171], v[102:105]
	v_mfma_f32_16x16x32_f16 v[98:101], v[158:161], v[168:171], v[98:101]
	v_mfma_f32_16x16x32_f16 v[126:129], v[140:143], v[176:179], v[126:129]
	v_mfma_f32_16x16x32_f16 v[122:125], v[158:161], v[176:179], v[122:125]
	v_mfma_f32_16x16x32_f16 v[118:121], v[140:143], v[188:191], v[118:121]
	v_mfma_f32_16x16x32_f16 v[114:117], v[158:161], v[188:191], v[114:117]
	v_mfma_f32_16x16x32_f16 v[110:113], v[140:143], v[196:199], v[110:113]
	v_mfma_f32_16x16x32_f16 v[106:109], v[158:161], v[196:199], v[106:109]
	v_mfma_f32_16x16x32_f16 v[102:105], v[154:157], v[172:175], v[102:105]
	v_mfma_f32_16x16x32_f16 v[98:101], v[164:167], v[172:175], v[98:101]
	v_mfma_f32_16x16x32_f16 v[126:129], v[154:157], v[184:187], v[126:129]
	v_mfma_f32_16x16x32_f16 v[122:125], v[164:167], v[184:187], v[122:125]
	v_mfma_f32_16x16x32_f16 v[118:121], v[154:157], v[192:195], v[118:121]
	v_mfma_f32_16x16x32_f16 v[114:117], v[164:167], v[192:195], v[114:117]
	v_mfma_f32_16x16x32_f16 v[110:113], v[154:157], v[200:203], v[110:113]
	v_mfma_f32_16x16x32_f16 v[106:109], v[164:167], v[200:203], v[106:109]
	s_barrier
	ds_read_b128 v[204:207], v137
	ds_read_b128 v[208:211], v137 offset:1024
	ds_read_b128 v[212:215], v137 offset:2048
	ds_read_b128 v[216:219], v137 offset:3072
	s_barrier
	s_waitcnt lgkmcnt(0)
	v_mfma_f32_16x16x32_f16 v[94:97], v[204:207], v[168:171], v[94:97]
	v_mfma_f32_16x16x32_f16 v[94:97], v[208:211], v[172:175], v[94:97]
	v_mfma_f32_16x16x32_f16 v[90:93], v[212:215], v[168:171], v[90:93]
	v_mfma_f32_16x16x32_f16 v[86:89], v[204:207], v[176:179], v[86:89]
	v_mfma_f32_16x16x32_f16 v[82:85], v[212:215], v[176:179], v[82:85]
	v_mfma_f32_16x16x32_f16 v[78:81], v[204:207], v[188:191], v[78:81]
	v_mfma_f32_16x16x32_f16 v[74:77], v[212:215], v[188:191], v[74:77]
	v_mfma_f32_16x16x32_f16 v[70:73], v[204:207], v[196:199], v[70:73]
	v_mfma_f32_16x16x32_f16 v[66:69], v[212:215], v[196:199], v[66:69]
	v_mfma_f32_16x16x32_f16 v[168:171], v[216:219], v[172:175], v[90:93]
	v_mfma_f32_16x16x32_f16 v[172:175], v[208:211], v[184:187], v[86:89]
	v_mfma_f32_16x16x32_f16 v[176:179], v[216:219], v[184:187], v[82:85]
	v_mfma_f32_16x16x32_f16 v[184:187], v[208:211], v[192:195], v[78:81]
	v_mfma_f32_16x16x32_f16 v[188:191], v[216:219], v[192:195], v[74:77]
	v_mfma_f32_16x16x32_f16 v[192:195], v[208:211], v[200:203], v[70:73]
	v_mfma_f32_16x16x32_f16 v[196:199], v[216:219], v[200:203], v[66:69]
	s_barrier
	s_nop 0
	ds_read_b128 v[66:69], v134 offset:16384
	ds_read_b128 v[70:73], v134 offset:17408
	ds_read_b128 v[74:77], v133 offset:16384
	ds_read_b128 v[78:81], v133 offset:17408
	ds_read_b128 v[82:85], v131 offset:16384
	ds_read_b128 v[86:89], v131 offset:17408
	ds_read_b128 v[90:93], v130 offset:16384
	ds_read_b128 v[200:203], v130 offset:17408
	s_waitcnt vmcnt(4)
	s_barrier
	s_waitcnt lgkmcnt(0)
	v_mfma_f32_16x16x32_f16 v[62:65], v[140:143], v[66:69], v[62:65]
	v_mfma_f32_16x16x32_f16 v[58:61], v[158:161], v[66:69], v[58:61]
	v_mfma_f32_16x16x32_f16 v[54:57], v[140:143], v[74:77], v[54:57]
	v_mfma_f32_16x16x32_f16 v[50:53], v[158:161], v[74:77], v[50:53]
	v_mfma_f32_16x16x32_f16 v[46:49], v[140:143], v[82:85], v[46:49]
	v_mfma_f32_16x16x32_f16 v[42:45], v[158:161], v[82:85], v[42:45]
	v_mfma_f32_16x16x32_f16 v[38:41], v[140:143], v[90:93], v[38:41]
	v_mfma_f32_16x16x32_f16 v[62:65], v[154:157], v[70:73], v[62:65]
	v_mfma_f32_16x16x32_f16 v[58:61], v[164:167], v[70:73], v[58:61]
	v_mfma_f32_16x16x32_f16 v[54:57], v[154:157], v[78:81], v[54:57]
	v_mfma_f32_16x16x32_f16 v[50:53], v[164:167], v[78:81], v[50:53]
	v_mfma_f32_16x16x32_f16 v[46:49], v[154:157], v[86:89], v[46:49]
	v_mfma_f32_16x16x32_f16 v[42:45], v[164:167], v[86:89], v[42:45]
	v_mfma_f32_16x16x32_f16 v[38:41], v[154:157], v[200:203], v[38:41]
	v_mfma_f32_16x16x32_f16 v[30:33], v[158:161], v[90:93], v[30:33]
	v_mfma_f32_16x16x32_f16 v[138:141], v[164:167], v[200:203], v[30:33]
	v_mfma_f32_16x16x32_f16 v[30:33], v[204:207], v[66:69], v[34:37]
	v_mfma_f32_16x16x32_f16 v[34:37], v[208:211], v[70:73], v[30:33]
	v_mfma_f32_16x16x32_f16 v[26:29], v[212:215], v[66:69], v[26:29]
	v_mfma_f32_16x16x32_f16 v[22:25], v[204:207], v[74:77], v[22:25]
	v_mfma_f32_16x16x32_f16 v[18:21], v[212:215], v[74:77], v[18:21]
	v_mfma_f32_16x16x32_f16 v[14:17], v[204:207], v[82:85], v[14:17]
	v_mfma_f32_16x16x32_f16 v[10:13], v[212:215], v[82:85], v[10:13]
	v_mfma_f32_16x16x32_f16 v[6:9], v[204:207], v[90:93], v[6:9]
	v_mfma_f32_16x16x32_f16 v[2:5], v[212:215], v[90:93], v[2:5]
	v_mfma_f32_16x16x32_f16 v[142:145], v[216:219], v[70:73], v[26:29]
	v_mfma_f32_16x16x32_f16 v[154:157], v[208:211], v[78:81], v[22:25]
	v_mfma_f32_16x16x32_f16 v[158:161], v[216:219], v[78:81], v[18:21]
	v_mfma_f32_16x16x32_f16 v[164:167], v[208:211], v[86:89], v[14:17]
	v_mfma_f32_16x16x32_f16 v[220:223], v[216:219], v[86:89], v[10:13]
	v_mfma_f32_16x16x32_f16 v[204:207], v[208:211], v[200:203], v[6:9]
	v_mfma_f32_16x16x32_f16 v[200:203], v[216:219], v[200:203], v[2:5]
	s_barrier
	s_nop 0
	ds_read_b128 v[2:5], v136
	ds_read_b128 v[6:9], v136 offset:1024
	ds_read_b128 v[208:211], v136 offset:2048
	ds_read_b128 v[212:215], v136 offset:3072
	ds_read_b128 v[10:13], v134 offset:32768
	ds_read_b128 v[14:17], v134 offset:33792
	ds_read_b128 v[18:21], v133 offset:32768
	ds_read_b128 v[22:25], v133 offset:33792
	ds_read_b128 v[26:29], v131 offset:32768
	ds_read_b128 v[30:33], v131 offset:33792
	ds_read_b128 v[216:219], v130 offset:32768
	ds_read_b128 v[224:227], v130 offset:33792
	s_waitcnt vmcnt(2)
	s_barrier
	s_waitcnt lgkmcnt(0)
	v_mfma_f32_16x16x32_f16 v[66:69], v[2:5], v[10:13], v[102:105]
	v_mfma_f32_16x16x32_f16 v[90:93], v[6:9], v[14:17], v[66:69]
	v_mfma_f32_16x16x32_f16 v[66:69], v[208:211], v[10:13], v[98:101]
	v_mfma_f32_16x16x32_f16 v[98:101], v[212:215], v[14:17], v[66:69]
	v_mfma_f32_16x16x32_f16 v[66:69], v[2:5], v[18:21], v[126:129]
	v_mfma_f32_16x16x32_f16 v[82:85], v[6:9], v[22:25], v[66:69]
	v_mfma_f32_16x16x32_f16 v[66:69], v[208:211], v[18:21], v[122:125]
	v_mfma_f32_16x16x32_f16 v[86:89], v[212:215], v[22:25], v[66:69]
	v_mfma_f32_16x16x32_f16 v[66:69], v[2:5], v[26:29], v[118:121]
	v_mfma_f32_16x16x32_f16 v[74:77], v[6:9], v[30:33], v[66:69]
	v_mfma_f32_16x16x32_f16 v[66:69], v[208:211], v[26:29], v[114:117]
	v_mfma_f32_16x16x32_f16 v[78:81], v[212:215], v[30:33], v[66:69]
	v_mfma_f32_16x16x32_f16 v[66:69], v[2:5], v[216:219], v[110:113]
	v_mfma_f32_16x16x32_f16 v[70:73], v[208:211], v[216:219], v[106:109]
	v_mfma_f32_16x16x32_f16 v[66:69], v[6:9], v[224:227], v[66:69]
	v_mfma_f32_16x16x32_f16 v[70:73], v[212:215], v[224:227], v[70:73]
	s_barrier
	ds_read_b128 v[228:231], v135
	ds_read_b128 v[232:235], v135 offset:1024
	ds_read_b128 v[236:239], v135 offset:2048
	ds_read_b128 v[240:243], v135 offset:3072
	s_waitcnt vmcnt(0)
	s_barrier
	s_waitcnt lgkmcnt(0)
	v_mfma_f32_16x16x32_f16 v[94:97], v[228:231], v[10:13], v[94:97]
	v_mfma_f32_16x16x32_f16 v[10:13], v[236:239], v[10:13], v[168:171]
	v_mfma_f32_16x16x32_f16 v[126:129], v[240:243], v[14:17], v[10:13]
	v_mfma_f32_16x16x32_f16 v[10:13], v[228:231], v[18:21], v[172:175]
	v_mfma_f32_16x16x32_f16 v[114:117], v[232:235], v[22:25], v[10:13]
	v_mfma_f32_16x16x32_f16 v[10:13], v[236:239], v[18:21], v[176:179]
	v_mfma_f32_16x16x32_f16 v[118:121], v[240:243], v[22:25], v[10:13]
	v_mfma_f32_16x16x32_f16 v[10:13], v[228:231], v[26:29], v[184:187]
	v_mfma_f32_16x16x32_f16 v[106:109], v[232:235], v[30:33], v[10:13]
	v_mfma_f32_16x16x32_f16 v[10:13], v[236:239], v[26:29], v[188:191]
	v_mfma_f32_16x16x32_f16 v[110:113], v[240:243], v[30:33], v[10:13]
	v_mfma_f32_16x16x32_f16 v[10:13], v[228:231], v[216:219], v[192:195]
	v_mfma_f32_16x16x32_f16 v[122:125], v[232:235], v[14:17], v[94:97]
	v_mfma_f32_16x16x32_f16 v[94:97], v[232:235], v[224:227], v[10:13]
	v_mfma_f32_16x16x32_f16 v[10:13], v[236:239], v[216:219], v[196:199]
	v_mfma_f32_16x16x32_f16 v[102:105], v[240:243], v[224:227], v[10:13]
	s_barrier
	ds_read_b128 v[168:171], v134 offset:49152
	ds_read_b128 v[134:137], v134 offset:50176
	ds_read_b128 v[172:175], v133 offset:49152
	ds_read_b128 v[176:179], v133 offset:50176
	ds_read_b128 v[184:187], v131 offset:49152
	ds_read_b128 v[188:191], v131 offset:50176
	ds_read_b128 v[192:195], v130 offset:49152
	ds_read_b128 v[196:199], v130 offset:50176
	s_barrier
	s_waitcnt lgkmcnt(0)
	v_mfma_f32_16x16x32_f16 v[10:13], v[2:5], v[168:171], v[62:65]
	v_mfma_f32_16x16x32_f16 v[26:29], v[6:9], v[134:137], v[10:13]
	v_mfma_f32_16x16x32_f16 v[10:13], v[208:211], v[168:171], v[58:61]
	v_mfma_f32_16x16x32_f16 v[30:33], v[212:215], v[134:137], v[10:13]
	v_mfma_f32_16x16x32_f16 v[10:13], v[2:5], v[172:175], v[54:57]
	v_mfma_f32_16x16x32_f16 v[18:21], v[6:9], v[176:179], v[10:13]
	v_mfma_f32_16x16x32_f16 v[10:13], v[208:211], v[172:175], v[50:53]
	v_mfma_f32_16x16x32_f16 v[22:25], v[212:215], v[176:179], v[10:13]
	v_mfma_f32_16x16x32_f16 v[10:13], v[2:5], v[184:187], v[46:49]
	v_mfma_f32_16x16x32_f16 v[2:5], v[2:5], v[192:195], v[38:41]
	v_mfma_f32_16x16x32_f16 v[10:13], v[6:9], v[188:191], v[10:13]
	v_mfma_f32_16x16x32_f16 v[14:17], v[208:211], v[184:187], v[42:45]
	v_mfma_f32_16x16x32_f16 v[2:5], v[6:9], v[196:199], v[2:5]
	v_mfma_f32_16x16x32_f16 v[6:9], v[208:211], v[192:195], v[138:141]
	v_mfma_f32_16x16x32_f16 v[14:17], v[212:215], v[188:191], v[14:17]
	v_mfma_f32_16x16x32_f16 v[6:9], v[212:215], v[196:199], v[6:9]
	v_mfma_f32_16x16x32_f16 v[34:37], v[228:231], v[168:171], v[34:37]
	v_mfma_f32_16x16x32_f16 v[58:61], v[232:235], v[134:137], v[34:37]
	v_mfma_f32_16x16x32_f16 v[34:37], v[236:239], v[168:171], v[142:145]
	v_mfma_f32_16x16x32_f16 v[62:65], v[240:243], v[134:137], v[34:37]
	v_mfma_f32_16x16x32_f16 v[34:37], v[228:231], v[172:175], v[154:157]
	v_mfma_f32_16x16x32_f16 v[50:53], v[232:235], v[176:179], v[34:37]
	v_mfma_f32_16x16x32_f16 v[34:37], v[236:239], v[172:175], v[158:161]
	v_mfma_f32_16x16x32_f16 v[54:57], v[240:243], v[176:179], v[34:37]
	v_mfma_f32_16x16x32_f16 v[34:37], v[228:231], v[184:187], v[164:167]
	v_mfma_f32_16x16x32_f16 v[42:45], v[232:235], v[188:191], v[34:37]
	v_mfma_f32_16x16x32_f16 v[34:37], v[236:239], v[184:187], v[220:223]
	v_mfma_f32_16x16x32_f16 v[46:49], v[240:243], v[188:191], v[34:37]
	v_mfma_f32_16x16x32_f16 v[34:37], v[228:231], v[192:195], v[204:207]
	v_mfma_f32_16x16x32_f16 v[38:41], v[236:239], v[192:195], v[200:203]
	v_mfma_f32_16x16x32_f16 v[34:37], v[232:235], v[196:199], v[34:37]
	v_mfma_f32_16x16x32_f16 v[38:41], v[240:243], v[196:199], v[38:41]

.LBB2_382:
	ds_read_b128 v[152:155], v151
	ds_read_b128 v[156:159], v151 offset:1024
	ds_read_b128 v[164:167], v151 offset:2048
	ds_read_b128 v[168:171], v151 offset:3072
	s_lshl_b32 s58, s84, 7
	s_add_u32 s59, s24, s58
	s_addc_u32 s91, s25, 0
	s_add_u32 s92, s59, 0x80
	s_addc_u32 s93, s91, 0
	s_add_i32 s56, s52, 0xc000
	s_mov_b32 m0, s56
	s_add_i32 s33, s52, 0xe000
	ds_read_b128 v[172:175], v147
	ds_read_b128 v[176:179], v147 offset:1024
	ds_read_b128 v[184:187], v146
	ds_read_b128 v[188:191], v146 offset:1024
	ds_read_b128 v[192:195], v145
	ds_read_b128 v[196:199], v145 offset:1024
	ds_read_b128 v[200:203], v144
	ds_read_b128 v[204:207], v144 offset:1024
	global_load_lds_dwordx4 v132, s[92:93]
	s_mov_b32 m0, s33
	s_nop 0
	global_load_lds_dwordx4 v130, s[92:93]
	s_waitcnt lgkmcnt(8)
	s_barrier
	s_waitcnt lgkmcnt(0)
	v_mfma_f32_16x16x32_f16 v[126:129], v[152:155], v[172:175], v[126:129]
	v_mfma_f32_16x16x32_f16 v[122:125], v[164:167], v[172:175], v[122:125]
	v_mfma_f32_16x16x32_f16 v[118:121], v[152:155], v[184:187], v[118:121]
	v_mfma_f32_16x16x32_f16 v[114:117], v[164:167], v[184:187], v[114:117]
	v_mfma_f32_16x16x32_f16 v[110:113], v[152:155], v[192:195], v[110:113]
	v_mfma_f32_16x16x32_f16 v[106:109], v[164:167], v[192:195], v[106:109]
	v_mfma_f32_16x16x32_f16 v[102:105], v[152:155], v[200:203], v[102:105]
	v_mfma_f32_16x16x32_f16 v[98:101], v[164:167], v[200:203], v[98:101]
	v_mfma_f32_16x16x32_f16 v[126:129], v[156:159], v[176:179], v[126:129]
	v_mfma_f32_16x16x32_f16 v[122:125], v[168:171], v[176:179], v[122:125]
	v_mfma_f32_16x16x32_f16 v[118:121], v[156:159], v[188:191], v[118:121]
	v_mfma_f32_16x16x32_f16 v[114:117], v[168:171], v[188:191], v[114:117]
	v_mfma_f32_16x16x32_f16 v[110:113], v[156:159], v[196:199], v[110:113]
	v_mfma_f32_16x16x32_f16 v[106:109], v[168:171], v[196:199], v[106:109]
	v_mfma_f32_16x16x32_f16 v[102:105], v[156:159], v[204:207], v[102:105]
	v_mfma_f32_16x16x32_f16 v[98:101], v[168:171], v[204:207], v[98:101]
	s_barrier
	s_add_i32 s57, s84, 2
	s_lshl_b32 s82, s57, 7
	s_add_u32 s92, s4, s82
	s_addc_u32 s93, s5, 0
	s_mov_b32 m0, s53
	ds_read_b128 v[208:211], v150
	ds_read_b128 v[212:215], v150 offset:1024
	ds_read_b128 v[216:219], v150 offset:2048
	ds_read_b128 v[220:223], v150 offset:3072
	global_load_lds_dwordx4 v162, s[92:93]
	s_mov_b32 m0, s55
	s_add_u32 s92, s92, 0x40000
	s_addc_u32 s93, s93, 0
	global_load_lds_dwordx4 v162, s[92:93]
	s_barrier
	s_waitcnt lgkmcnt(0)
	v_mfma_f32_16x16x32_f16 v[94:97], v[208:211], v[172:175], v[94:97]
	v_mfma_f32_16x16x32_f16 v[90:93], v[216:219], v[172:175], v[90:93]
	v_mfma_f32_16x16x32_f16 v[86:89], v[208:211], v[184:187], v[86:89]
	v_mfma_f32_16x16x32_f16 v[82:85], v[216:219], v[184:187], v[82:85]
	v_mfma_f32_16x16x32_f16 v[78:81], v[208:211], v[192:195], v[78:81]
	v_mfma_f32_16x16x32_f16 v[74:77], v[216:219], v[192:195], v[74:77]
	v_mfma_f32_16x16x32_f16 v[70:73], v[208:211], v[200:203], v[70:73]
	v_mfma_f32_16x16x32_f16 v[66:69], v[216:219], v[200:203], v[66:69]
	v_mfma_f32_16x16x32_f16 v[94:97], v[212:215], v[176:179], v[94:97]
	v_mfma_f32_16x16x32_f16 v[90:93], v[220:223], v[176:179], v[90:93]
	v_mfma_f32_16x16x32_f16 v[86:89], v[212:215], v[188:191], v[86:89]
	v_mfma_f32_16x16x32_f16 v[82:85], v[220:223], v[188:191], v[82:85]
	v_mfma_f32_16x16x32_f16 v[78:81], v[212:215], v[196:199], v[78:81]
	v_mfma_f32_16x16x32_f16 v[74:77], v[220:223], v[196:199], v[74:77]
	v_mfma_f32_16x16x32_f16 v[70:73], v[212:215], v[204:207], v[70:73]
	v_mfma_f32_16x16x32_f16 v[66:69], v[220:223], v[204:207], v[66:69]
	s_add_u32 s92, s24, s82
	s_addc_u32 s93, s25, 0
	s_mov_b32 m0, s52
	s_barrier
	ds_read_b128 v[172:175], v147 offset:16384
	ds_read_b128 v[176:179], v147 offset:17408
	ds_read_b128 v[184:187], v146 offset:16384
	ds_read_b128 v[188:191], v146 offset:17408
	ds_read_b128 v[192:195], v145 offset:16384
	ds_read_b128 v[196:199], v145 offset:17408
	ds_read_b128 v[200:203], v144 offset:16384
	ds_read_b128 v[204:207], v144 offset:17408
	global_load_lds_dwordx4 v134, s[92:93]
	s_mov_b32 m0, s86
	s_nop 0
	global_load_lds_dwordx4 v136, s[92:93]
	s_barrier
	s_waitcnt lgkmcnt(0)
	v_mfma_f32_16x16x32_f16 v[62:65], v[152:155], v[172:175], v[62:65]
	v_mfma_f32_16x16x32_f16 v[58:61], v[164:167], v[172:175], v[58:61]
	v_mfma_f32_16x16x32_f16 v[54:57], v[152:155], v[184:187], v[54:57]
	v_mfma_f32_16x16x32_f16 v[50:53], v[164:167], v[184:187], v[50:53]
	v_mfma_f32_16x16x32_f16 v[46:49], v[152:155], v[192:195], v[46:49]
	v_mfma_f32_16x16x32_f16 v[42:45], v[164:167], v[192:195], v[42:45]
	v_mfma_f32_16x16x32_f16 v[38:41], v[152:155], v[200:203], v[38:41]
	v_mfma_f32_16x16x32_f16 v[34:37], v[164:167], v[200:203], v[34:37]
	v_mfma_f32_16x16x32_f16 v[62:65], v[156:159], v[176:179], v[62:65]
	v_mfma_f32_16x16x32_f16 v[58:61], v[168:171], v[176:179], v[58:61]
	v_mfma_f32_16x16x32_f16 v[54:57], v[156:159], v[188:191], v[54:57]
	v_mfma_f32_16x16x32_f16 v[50:53], v[168:171], v[188:191], v[50:53]
	v_mfma_f32_16x16x32_f16 v[46:49], v[156:159], v[196:199], v[46:49]
	v_mfma_f32_16x16x32_f16 v[42:45], v[168:171], v[196:199], v[42:45]
	v_mfma_f32_16x16x32_f16 v[38:41], v[156:159], v[204:207], v[38:41]
	v_mfma_f32_16x16x32_f16 v[34:37], v[168:171], v[204:207], v[34:37]
	s_barrier
	s_add_u32 s94, s10, s82
	s_addc_u32 s95, s11, 0
	s_mov_b32 m0, s87
	s_nop 0
	global_load_lds_dwordx4 v162, s[94:95]
	s_mov_b32 m0, s88
	s_add_u32 s94, s94, 0x40000
	s_addc_u32 s95, s95, 0
	global_load_lds_dwordx4 v162, s[94:95]
	s_waitcnt vmcnt(6)
	s_barrier
	v_mfma_f32_16x16x32_f16 v[30:33], v[208:211], v[172:175], v[30:33]
	v_mfma_f32_16x16x32_f16 v[26:29], v[216:219], v[172:175], v[26:29]
	v_mfma_f32_16x16x32_f16 v[22:25], v[208:211], v[184:187], v[22:25]
	v_mfma_f32_16x16x32_f16 v[18:21], v[216:219], v[184:187], v[18:21]
	v_mfma_f32_16x16x32_f16 v[14:17], v[208:211], v[192:195], v[14:17]
	v_mfma_f32_16x16x32_f16 v[10:13], v[216:219], v[192:195], v[10:13]
	v_mfma_f32_16x16x32_f16 v[6:9], v[208:211], v[200:203], v[6:9]
	v_mfma_f32_16x16x32_f16 v[2:5], v[216:219], v[200:203], v[2:5]
	v_mfma_f32_16x16x32_f16 v[30:33], v[212:215], v[176:179], v[30:33]
	v_mfma_f32_16x16x32_f16 v[26:29], v[220:223], v[176:179], v[26:29]
	v_mfma_f32_16x16x32_f16 v[22:25], v[212:215], v[188:191], v[22:25]
	v_mfma_f32_16x16x32_f16 v[18:21], v[220:223], v[188:191], v[18:21]
	v_mfma_f32_16x16x32_f16 v[14:17], v[212:215], v[196:199], v[14:17]
	v_mfma_f32_16x16x32_f16 v[10:13], v[220:223], v[196:199], v[10:13]
	v_mfma_f32_16x16x32_f16 v[6:9], v[212:215], v[204:207], v[6:9]
	v_mfma_f32_16x16x32_f16 v[2:5], v[220:223], v[204:207], v[2:5]
	s_barrier
	ds_read_b128 v[152:155], v149
	ds_read_b128 v[156:159], v149 offset:1024
	ds_read_b128 v[164:167], v149 offset:2048
	ds_read_b128 v[168:171], v149 offset:3072
	s_mov_b32 m0, s89
	ds_read_b128 v[172:175], v147 offset:32768
	ds_read_b128 v[176:179], v147 offset:33792
	ds_read_b128 v[184:187], v146 offset:32768
	ds_read_b128 v[188:191], v146 offset:33792
	ds_read_b128 v[192:195], v145 offset:32768
	ds_read_b128 v[196:199], v145 offset:33792
	ds_read_b128 v[200:203], v144 offset:32768
	ds_read_b128 v[204:207], v144 offset:33792
	global_load_lds_dwordx4 v132, s[92:93]
	s_mov_b32 m0, s90
	s_nop 0
	global_load_lds_dwordx4 v130, s[92:93]
	s_waitcnt lgkmcnt(8)
	s_barrier
	s_waitcnt lgkmcnt(0)
	v_mfma_f32_16x16x32_f16 v[126:129], v[152:155], v[172:175], v[126:129]
	v_mfma_f32_16x16x32_f16 v[122:125], v[164:167], v[172:175], v[122:125]
	v_mfma_f32_16x16x32_f16 v[118:121], v[152:155], v[184:187], v[118:121]
	v_mfma_f32_16x16x32_f16 v[114:117], v[164:167], v[184:187], v[114:117]
	v_mfma_f32_16x16x32_f16 v[110:113], v[152:155], v[192:195], v[110:113]
	v_mfma_f32_16x16x32_f16 v[106:109], v[164:167], v[192:195], v[106:109]
	v_mfma_f32_16x16x32_f16 v[102:105], v[152:155], v[200:203], v[102:105]
	v_mfma_f32_16x16x32_f16 v[98:101], v[164:167], v[200:203], v[98:101]
	v_mfma_f32_16x16x32_f16 v[126:129], v[156:159], v[176:179], v[126:129]
	v_mfma_f32_16x16x32_f16 v[122:125], v[168:171], v[176:179], v[122:125]
	v_mfma_f32_16x16x32_f16 v[118:121], v[156:159], v[188:191], v[118:121]
	v_mfma_f32_16x16x32_f16 v[114:117], v[168:171], v[188:191], v[114:117]
	v_mfma_f32_16x16x32_f16 v[110:113], v[156:159], v[196:199], v[110:113]
	v_mfma_f32_16x16x32_f16 v[106:109], v[168:171], v[196:199], v[106:109]
	v_mfma_f32_16x16x32_f16 v[102:105], v[156:159], v[204:207], v[102:105]
	v_mfma_f32_16x16x32_f16 v[98:101], v[168:171], v[204:207], v[98:101]
	s_barrier
	s_add_u32 s82, s4, s58
	s_addc_u32 s83, s5, 0
	s_add_u32 s92, s82, 0x180
	s_addc_u32 s93, s83, 0
	s_add_i32 m0, s52, 0x18000
	ds_read_b128 v[208:211], v148
	ds_read_b128 v[212:215], v148 offset:1024
	ds_read_b128 v[216:219], v148 offset:2048
	ds_read_b128 v[220:223], v148 offset:3072
	global_load_lds_dwordx4 v162, s[92:93]
	s_add_i32 m0, s52, 0x1a000
	s_add_u32 s92, s92, 0x40000
	s_addc_u32 s93, s93, 0
	global_load_lds_dwordx4 v162, s[92:93]
	s_barrier
	s_waitcnt lgkmcnt(0)
	v_mfma_f32_16x16x32_f16 v[94:97], v[208:211], v[172:175], v[94:97]
	v_mfma_f32_16x16x32_f16 v[90:93], v[216:219], v[172:175], v[90:93]
	v_mfma_f32_16x16x32_f16 v[86:89], v[208:211], v[184:187], v[86:89]
	v_mfma_f32_16x16x32_f16 v[82:85], v[216:219], v[184:187], v[82:85]
	v_mfma_f32_16x16x32_f16 v[78:81], v[208:211], v[192:195], v[78:81]
	v_mfma_f32_16x16x32_f16 v[74:77], v[216:219], v[192:195], v[74:77]
	v_mfma_f32_16x16x32_f16 v[70:73], v[208:211], v[200:203], v[70:73]
	v_mfma_f32_16x16x32_f16 v[66:69], v[216:219], v[200:203], v[66:69]
	v_mfma_f32_16x16x32_f16 v[94:97], v[212:215], v[176:179], v[94:97]
	v_mfma_f32_16x16x32_f16 v[90:93], v[220:223], v[176:179], v[90:93]
	v_mfma_f32_16x16x32_f16 v[86:89], v[212:215], v[188:191], v[86:89]
	v_mfma_f32_16x16x32_f16 v[82:85], v[220:223], v[188:191], v[82:85]
	v_mfma_f32_16x16x32_f16 v[78:81], v[212:215], v[196:199], v[78:81]
	v_mfma_f32_16x16x32_f16 v[74:77], v[220:223], v[196:199], v[74:77]
	v_mfma_f32_16x16x32_f16 v[70:73], v[212:215], v[204:207], v[70:73]
	v_mfma_f32_16x16x32_f16 v[66:69], v[220:223], v[204:207], v[66:69]
	s_add_u32 s92, s59, 0x180
	s_addc_u32 s93, s91, 0
	s_mov_b32 m0, s34
	s_barrier
	ds_read_b128 v[172:175], v147 offset:49152
	ds_read_b128 v[176:179], v147 offset:50176
	ds_read_b128 v[184:187], v146 offset:49152
	ds_read_b128 v[188:191], v146 offset:50176
	ds_read_b128 v[192:195], v145 offset:49152
	ds_read_b128 v[196:199], v145 offset:50176
	ds_read_b128 v[200:203], v144 offset:49152
	ds_read_b128 v[204:207], v144 offset:50176
	global_load_lds_dwordx4 v134, s[92:93]
	s_mov_b32 m0, s35
	s_nop 0
	global_load_lds_dwordx4 v136, s[92:93]
	s_barrier
	s_waitcnt lgkmcnt(0)
	v_mfma_f32_16x16x32_f16 v[62:65], v[152:155], v[172:175], v[62:65]
	v_mfma_f32_16x16x32_f16 v[58:61], v[164:167], v[172:175], v[58:61]
	v_mfma_f32_16x16x32_f16 v[54:57], v[152:155], v[184:187], v[54:57]
	v_mfma_f32_16x16x32_f16 v[50:53], v[164:167], v[184:187], v[50:53]
	v_mfma_f32_16x16x32_f16 v[46:49], v[152:155], v[192:195], v[46:49]
	v_mfma_f32_16x16x32_f16 v[42:45], v[164:167], v[192:195], v[42:45]
	v_mfma_f32_16x16x32_f16 v[38:41], v[152:155], v[200:203], v[38:41]
	v_mfma_f32_16x16x32_f16 v[34:37], v[164:167], v[200:203], v[34:37]
	v_mfma_f32_16x16x32_f16 v[62:65], v[156:159], v[176:179], v[62:65]
	v_mfma_f32_16x16x32_f16 v[58:61], v[168:171], v[176:179], v[58:61]
	v_mfma_f32_16x16x32_f16 v[54:57], v[156:159], v[188:191], v[54:57]
	v_mfma_f32_16x16x32_f16 v[50:53], v[168:171], v[188:191], v[50:53]
	v_mfma_f32_16x16x32_f16 v[46:49], v[156:159], v[196:199], v[46:49]
	v_mfma_f32_16x16x32_f16 v[42:45], v[168:171], v[196:199], v[42:45]
	v_mfma_f32_16x16x32_f16 v[38:41], v[156:159], v[204:207], v[38:41]
	v_mfma_f32_16x16x32_f16 v[34:37], v[168:171], v[204:207], v[34:37]
	s_barrier
	s_add_u32 s58, s10, s58
	s_addc_u32 s59, s11, 0
	s_add_u32 s58, s58, 0x180
	s_addc_u32 s59, s59, 0
	s_add_i32 m0, s52, 0x1c000
	s_nop 0
	global_load_lds_dwordx4 v162, s[58:59]
	s_add_i32 m0, s52, 0x1e000
	s_add_u32 s58, s58, 0x40000
	s_addc_u32 s59, s59, 0
	global_load_lds_dwordx4 v162, s[58:59]
	s_waitcnt vmcnt(6)
	s_barrier
	v_mfma_f32_16x16x32_f16 v[30:33], v[208:211], v[172:175], v[30:33]
	v_mfma_f32_16x16x32_f16 v[26:29], v[216:219], v[172:175], v[26:29]
	v_mfma_f32_16x16x32_f16 v[22:25], v[208:211], v[184:187], v[22:25]
	v_mfma_f32_16x16x32_f16 v[18:21], v[216:219], v[184:187], v[18:21]
	v_mfma_f32_16x16x32_f16 v[14:17], v[208:211], v[192:195], v[14:17]
	v_mfma_f32_16x16x32_f16 v[10:13], v[216:219], v[192:195], v[10:13]
	v_mfma_f32_16x16x32_f16 v[6:9], v[208:211], v[200:203], v[6:9]
	v_mfma_f32_16x16x32_f16 v[2:5], v[216:219], v[200:203], v[2:5]
	v_mfma_f32_16x16x32_f16 v[30:33], v[212:215], v[176:179], v[30:33]
	v_mfma_f32_16x16x32_f16 v[26:29], v[220:223], v[176:179], v[26:29]
	v_mfma_f32_16x16x32_f16 v[22:25], v[212:215], v[188:191], v[22:25]
	v_mfma_f32_16x16x32_f16 v[18:21], v[220:223], v[188:191], v[18:21]
	v_mfma_f32_16x16x32_f16 v[14:17], v[212:215], v[196:199], v[14:17]
	v_mfma_f32_16x16x32_f16 v[10:13], v[220:223], v[196:199], v[10:13]
	v_mfma_f32_16x16x32_f16 v[6:9], v[212:215], v[204:207], v[6:9]
	v_mfma_f32_16x16x32_f16 v[2:5], v[220:223], v[204:207], v[2:5]
	s_cmp_lt_u32 s84, 28
	s_mov_b32 s84, s57
	s_barrier
	s_cbranch_scc1 .LBB2_382
	v_readlane_b32 s4, v244, 8
	v_readlane_b32 s5, v244, 9
	s_mov_b32 m0, s56
	ds_read_b128 v[134:137], v151
	ds_read_b128 v[152:155], v151 offset:1024
	ds_read_b128 v[156:159], v151 offset:2048
	ds_read_b128 v[164:167], v151 offset:3072
	ds_read_b128 v[168:171], v147
	ds_read_b128 v[172:175], v147 offset:1024
	ds_read_b128 v[176:179], v146
	ds_read_b128 v[184:187], v146 offset:1024
	ds_read_b128 v[188:191], v145
	ds_read_b128 v[192:195], v145 offset:1024
	ds_read_b128 v[196:199], v144
	ds_read_b128 v[200:203], v144 offset:1024
	v_lshl_add_u64 v[132:133], s[4:5], 0, v[132:133]
	global_load_lds_dwordx4 v[132:133], off
	v_lshl_add_u64 v[130:131], s[4:5], 0, v[130:131]
	s_mov_b32 m0, s33
	s_nop 0
	global_load_lds_dwordx4 v[130:131], off
	s_barrier
	s_waitcnt lgkmcnt(0)
	v_mfma_f32_16x16x32_f16 v[126:129], v[134:137], v[168:171], v[126:129]
	v_mfma_f32_16x16x32_f16 v[122:125], v[156:159], v[168:171], v[122:125]
	v_mfma_f32_16x16x32_f16 v[110:113], v[134:137], v[188:191], v[110:113]
	v_mfma_f32_16x16x32_f16 v[106:109], v[156:159], v[188:191], v[106:109]
	v_mfma_f32_16x16x32_f16 v[126:129], v[152:155], v[172:175], v[126:129]
	v_mfma_f32_16x16x32_f16 v[122:125], v[164:167], v[172:175], v[122:125]
	v_mfma_f32_16x16x32_f16 v[118:121], v[134:137], v[176:179], v[118:121]
	v_mfma_f32_16x16x32_f16 v[114:117], v[156:159], v[176:179], v[114:117]
	v_mfma_f32_16x16x32_f16 v[110:113], v[152:155], v[192:195], v[110:113]
	v_mfma_f32_16x16x32_f16 v[106:109], v[164:167], v[192:195], v[106:109]
	v_mfma_f32_16x16x32_f16 v[102:105], v[134:137], v[196:199], v[102:105]
	v_mfma_f32_16x16x32_f16 v[98:101], v[156:159], v[196:199], v[98:101]
	v_mfma_f32_16x16x32_f16 v[130:133], v[152:155], v[184:187], v[118:121]
	v_mfma_f32_16x16x32_f16 v[204:207], v[164:167], v[184:187], v[114:117]
	v_mfma_f32_16x16x32_f16 v[208:211], v[152:155], v[200:203], v[102:105]
	v_mfma_f32_16x16x32_f16 v[212:215], v[164:167], v[200:203], v[98:101]
	s_barrier
	s_nop 1
	ds_read_b128 v[98:101], v150
	ds_read_b128 v[102:105], v150 offset:1024
	ds_read_b128 v[114:117], v150 offset:2048
	ds_read_b128 v[118:121], v150 offset:3072
	s_barrier
	s_waitcnt lgkmcnt(0)
	v_mfma_f32_16x16x32_f16 v[94:97], v[98:101], v[168:171], v[94:97]
	v_mfma_f32_16x16x32_f16 v[90:93], v[114:117], v[168:171], v[90:93]
	v_mfma_f32_16x16x32_f16 v[78:81], v[98:101], v[188:191], v[78:81]
	v_mfma_f32_16x16x32_f16 v[74:77], v[114:117], v[188:191], v[74:77]
	v_mfma_f32_16x16x32_f16 v[94:97], v[102:105], v[172:175], v[94:97]
	v_mfma_f32_16x16x32_f16 v[90:93], v[118:121], v[172:175], v[90:93]
	v_mfma_f32_16x16x32_f16 v[86:89], v[98:101], v[176:179], v[86:89]
	v_mfma_f32_16x16x32_f16 v[82:85], v[114:117], v[176:179], v[82:85]
	v_mfma_f32_16x16x32_f16 v[78:81], v[102:105], v[192:195], v[78:81]
	v_mfma_f32_16x16x32_f16 v[74:77], v[118:121], v[192:195], v[74:77]
	v_mfma_f32_16x16x32_f16 v[70:73], v[98:101], v[196:199], v[70:73]
	v_mfma_f32_16x16x32_f16 v[66:69], v[114:117], v[196:199], v[66:69]
	v_mfma_f32_16x16x32_f16 v[168:171], v[102:105], v[184:187], v[86:89]
	v_mfma_f32_16x16x32_f16 v[172:175], v[118:121], v[184:187], v[82:85]
	v_mfma_f32_16x16x32_f16 v[176:179], v[102:105], v[200:203], v[70:73]
	v_mfma_f32_16x16x32_f16 v[184:187], v[118:121], v[200:203], v[66:69]
	s_barrier
	s_nop 1
	ds_read_b128 v[66:69], v147 offset:16384
	ds_read_b128 v[70:73], v147 offset:17408
	ds_read_b128 v[82:85], v146 offset:16384
	ds_read_b128 v[86:89], v146 offset:17408
	ds_read_b128 v[188:191], v145 offset:16384
	ds_read_b128 v[192:195], v145 offset:17408
	ds_read_b128 v[196:199], v144 offset:16384
	ds_read_b128 v[200:203], v144 offset:17408
	s_waitcnt vmcnt(4)
	s_barrier
	s_waitcnt lgkmcnt(0)
	v_mfma_f32_16x16x32_f16 v[62:65], v[134:137], v[66:69], v[62:65]
	v_mfma_f32_16x16x32_f16 v[58:61], v[156:159], v[66:69], v[58:61]
	v_mfma_f32_16x16x32_f16 v[46:49], v[134:137], v[188:191], v[46:49]
	v_mfma_f32_16x16x32_f16 v[42:45], v[156:159], v[188:191], v[42:45]
	v_mfma_f32_16x16x32_f16 v[62:65], v[152:155], v[70:73], v[62:65]
	v_mfma_f32_16x16x32_f16 v[58:61], v[164:167], v[70:73], v[58:61]
	v_mfma_f32_16x16x32_f16 v[54:57], v[134:137], v[82:85], v[54:57]
	v_mfma_f32_16x16x32_f16 v[50:53], v[156:159], v[82:85], v[50:53]
	v_mfma_f32_16x16x32_f16 v[46:49], v[152:155], v[192:195], v[46:49]
	v_mfma_f32_16x16x32_f16 v[42:45], v[164:167], v[192:195], v[42:45]
	v_mfma_f32_16x16x32_f16 v[38:41], v[134:137], v[196:199], v[38:41]
	v_mfma_f32_16x16x32_f16 v[34:37], v[156:159], v[196:199], v[34:37]
	v_mfma_f32_16x16x32_f16 v[216:219], v[152:155], v[86:89], v[54:57]
	v_mfma_f32_16x16x32_f16 v[220:223], v[164:167], v[86:89], v[50:53]
	v_mfma_f32_16x16x32_f16 v[134:137], v[152:155], v[200:203], v[38:41]
	v_mfma_f32_16x16x32_f16 v[150:153], v[164:167], v[200:203], v[34:37]
	v_mfma_f32_16x16x32_f16 v[30:33], v[98:101], v[66:69], v[30:33]
	v_mfma_f32_16x16x32_f16 v[26:29], v[114:117], v[66:69], v[26:29]
	v_mfma_f32_16x16x32_f16 v[14:17], v[98:101], v[188:191], v[14:17]
	v_mfma_f32_16x16x32_f16 v[10:13], v[114:117], v[188:191], v[10:13]
	v_mfma_f32_16x16x32_f16 v[30:33], v[102:105], v[70:73], v[30:33]
	v_mfma_f32_16x16x32_f16 v[26:29], v[118:121], v[70:73], v[26:29]
	v_mfma_f32_16x16x32_f16 v[22:25], v[98:101], v[82:85], v[22:25]
	v_mfma_f32_16x16x32_f16 v[18:21], v[114:117], v[82:85], v[18:21]
	v_mfma_f32_16x16x32_f16 v[14:17], v[102:105], v[192:195], v[14:17]
	v_mfma_f32_16x16x32_f16 v[10:13], v[118:121], v[192:195], v[10:13]
	v_mfma_f32_16x16x32_f16 v[6:9], v[98:101], v[196:199], v[6:9]
	v_mfma_f32_16x16x32_f16 v[2:5], v[114:117], v[196:199], v[2:5]
	v_mfma_f32_16x16x32_f16 v[154:157], v[102:105], v[86:89], v[22:25]
	v_mfma_f32_16x16x32_f16 v[158:161], v[118:121], v[86:89], v[18:21]
	v_mfma_f32_16x16x32_f16 v[164:167], v[102:105], v[200:203], v[6:9]
	v_mfma_f32_16x16x32_f16 v[188:191], v[118:121], v[200:203], v[2:5]
	s_barrier
	s_nop 1
	ds_read_b128 v[2:5], v149
	ds_read_b128 v[6:9], v149 offset:1024
	ds_read_b128 v[192:195], v149 offset:2048
	ds_read_b128 v[196:199], v149 offset:3072
	ds_read_b128 v[18:21], v147 offset:32768
	ds_read_b128 v[22:25], v147 offset:33792
	ds_read_b128 v[34:37], v146 offset:32768
	ds_read_b128 v[38:41], v146 offset:33792
	ds_read_b128 v[50:53], v145 offset:32768
	ds_read_b128 v[54:57], v145 offset:33792
	ds_read_b128 v[200:203], v144 offset:32768
	ds_read_b128 v[224:227], v144 offset:33792
	s_waitcnt vmcnt(2)
	s_barrier
	s_waitcnt lgkmcnt(0)
	v_mfma_f32_16x16x32_f16 v[66:69], v[2:5], v[18:21], v[126:129]
	v_mfma_f32_16x16x32_f16 v[118:121], v[6:9], v[22:25], v[66:69]
	v_mfma_f32_16x16x32_f16 v[66:69], v[192:195], v[18:21], v[122:125]
	v_mfma_f32_16x16x32_f16 v[114:117], v[196:199], v[22:25], v[66:69]
	v_mfma_f32_16x16x32_f16 v[66:69], v[2:5], v[34:37], v[130:133]
	v_mfma_f32_16x16x32_f16 v[102:105], v[6:9], v[38:41], v[66:69]
	v_mfma_f32_16x16x32_f16 v[66:69], v[192:195], v[34:37], v[204:207]
	v_mfma_f32_16x16x32_f16 v[98:101], v[196:199], v[38:41], v[66:69]
	v_mfma_f32_16x16x32_f16 v[66:69], v[2:5], v[50:53], v[110:113]
	v_mfma_f32_16x16x32_f16 v[86:89], v[6:9], v[54:57], v[66:69]
	v_mfma_f32_16x16x32_f16 v[66:69], v[192:195], v[50:53], v[106:109]
	v_mfma_f32_16x16x32_f16 v[82:85], v[196:199], v[54:57], v[66:69]
	v_mfma_f32_16x16x32_f16 v[66:69], v[2:5], v[200:203], v[208:211]
	v_mfma_f32_16x16x32_f16 v[70:73], v[6:9], v[224:227], v[66:69]
	v_mfma_f32_16x16x32_f16 v[66:69], v[192:195], v[200:203], v[212:215]
	v_mfma_f32_16x16x32_f16 v[66:69], v[196:199], v[224:227], v[66:69]
	s_barrier
	ds_read_b128 v[130:133], v148
	ds_read_b128 v[204:207], v148 offset:1024
	ds_read_b128 v[208:211], v148 offset:2048
	ds_read_b128 v[212:215], v148 offset:3072
	s_waitcnt vmcnt(0)
	s_barrier
	s_waitcnt lgkmcnt(0)
	v_mfma_f32_16x16x32_f16 v[94:97], v[130:133], v[18:21], v[94:97]
	v_mfma_f32_16x16x32_f16 v[18:21], v[208:211], v[18:21], v[90:93]
	v_mfma_f32_16x16x32_f16 v[122:125], v[212:215], v[22:25], v[18:21]
	v_mfma_f32_16x16x32_f16 v[18:21], v[130:133], v[34:37], v[168:171]
	v_mfma_f32_16x16x32_f16 v[110:113], v[204:207], v[38:41], v[18:21]
	v_mfma_f32_16x16x32_f16 v[18:21], v[208:211], v[34:37], v[172:175]
	v_mfma_f32_16x16x32_f16 v[106:109], v[212:215], v[38:41], v[18:21]
	v_mfma_f32_16x16x32_f16 v[18:21], v[130:133], v[50:53], v[78:81]
	v_mfma_f32_16x16x32_f16 v[126:129], v[204:207], v[22:25], v[94:97]
	v_mfma_f32_16x16x32_f16 v[94:97], v[204:207], v[54:57], v[18:21]
	v_mfma_f32_16x16x32_f16 v[18:21], v[208:211], v[50:53], v[74:77]
	v_mfma_f32_16x16x32_f16 v[90:93], v[212:215], v[54:57], v[18:21]
	v_mfma_f32_16x16x32_f16 v[18:21], v[130:133], v[200:203], v[176:179]
	v_mfma_f32_16x16x32_f16 v[78:81], v[204:207], v[224:227], v[18:21]
	v_mfma_f32_16x16x32_f16 v[18:21], v[208:211], v[200:203], v[184:187]
	v_mfma_f32_16x16x32_f16 v[74:77], v[212:215], v[224:227], v[18:21]
	s_barrier
	ds_read_b128 v[168:171], v147 offset:49152
	ds_read_b128 v[172:175], v147 offset:50176
	ds_read_b128 v[176:179], v146 offset:49152
	ds_read_b128 v[146:149], v146 offset:50176
	ds_read_b128 v[184:187], v145 offset:49152
	ds_read_b128 v[200:203], v145 offset:50176
	ds_read_b128 v[224:227], v144 offset:49152
	ds_read_b128 v[228:231], v144 offset:50176
	s_barrier
	s_waitcnt lgkmcnt(0)
	v_mfma_f32_16x16x32_f16 v[18:21], v[2:5], v[168:171], v[62:65]
	v_mfma_f32_16x16x32_f16 v[54:57], v[6:9], v[172:175], v[18:21]
	v_mfma_f32_16x16x32_f16 v[18:21], v[192:195], v[168:171], v[58:61]
	v_mfma_f32_16x16x32_f16 v[50:53], v[196:199], v[172:175], v[18:21]
	v_mfma_f32_16x16x32_f16 v[18:21], v[2:5], v[176:179], v[216:219]
	v_mfma_f32_16x16x32_f16 v[38:41], v[6:9], v[146:149], v[18:21]
	v_mfma_f32_16x16x32_f16 v[18:21], v[192:195], v[176:179], v[220:223]
	v_mfma_f32_16x16x32_f16 v[34:37], v[196:199], v[146:149], v[18:21]
	v_mfma_f32_16x16x32_f16 v[18:21], v[2:5], v[184:187], v[46:49]
	v_mfma_f32_16x16x32_f16 v[2:5], v[2:5], v[224:227], v[134:137]
	v_mfma_f32_16x16x32_f16 v[22:25], v[6:9], v[200:203], v[18:21]
	v_mfma_f32_16x16x32_f16 v[18:21], v[192:195], v[184:187], v[42:45]
	v_mfma_f32_16x16x32_f16 v[6:9], v[6:9], v[228:231], v[2:5]
	v_mfma_f32_16x16x32_f16 v[2:5], v[192:195], v[224:227], v[150:153]
	v_mfma_f32_16x16x32_f16 v[18:21], v[196:199], v[200:203], v[18:21]
	v_mfma_f32_16x16x32_f16 v[2:5], v[196:199], v[228:231], v[2:5]
	v_mfma_f32_16x16x32_f16 v[26:29], v[208:211], v[168:171], v[26:29]
	v_mfma_f32_16x16x32_f16 v[58:61], v[212:215], v[172:175], v[26:29]
	v_mfma_f32_16x16x32_f16 v[26:29], v[130:133], v[176:179], v[154:157]
	v_mfma_f32_16x16x32_f16 v[46:49], v[204:207], v[146:149], v[26:29]
	v_mfma_f32_16x16x32_f16 v[26:29], v[208:211], v[176:179], v[158:161]
	v_mfma_f32_16x16x32_f16 v[10:13], v[208:211], v[184:187], v[10:13]
	v_mfma_f32_16x16x32_f16 v[30:33], v[130:133], v[168:171], v[30:33]
	v_mfma_f32_16x16x32_f16 v[42:45], v[212:215], v[146:149], v[26:29]
	v_mfma_f32_16x16x32_f16 v[14:17], v[130:133], v[184:187], v[14:17]
	v_mfma_f32_16x16x32_f16 v[26:29], v[212:215], v[200:203], v[10:13]
	v_mfma_f32_16x16x32_f16 v[10:13], v[130:133], v[224:227], v[164:167]
	v_mfma_f32_16x16x32_f16 v[62:65], v[204:207], v[172:175], v[30:33]
	v_mfma_f32_16x16x32_f16 v[30:33], v[204:207], v[200:203], v[14:17]
	v_mfma_f32_16x16x32_f16 v[14:17], v[204:207], v[228:231], v[10:13]
	v_mfma_f32_16x16x32_f16 v[10:13], v[208:211], v[224:227], v[188:191]
	v_mfma_f32_16x16x32_f16 v[10:13], v[212:215], v[228:231], v[10:13]
